# h1 stores of second-round strips written through (sc1), first-round strips plain
# baseline (speedup 1.0000x reference)
.Lw2b33:
	v_add_f32_e32 v21, 1.0, v21
	v_rcp_f32_e32 v28, v21
	v_add_f32_e32 v21, 1.0, v26
	v_pk_mul_f32 v[26:27], v[20:21], v[40:41] op_sel_hi:[0,1]
	v_pk_fma_f32 v[8:9], v[8:9], v[26:27], v[48:49]
	v_rcp_f32_e32 v29, v21
	v_pk_mul_f32 v[40:41], v[8:9], v[8:9]
	v_mad_u32_u24 v104, v86, 6, v83
	s_cmp_ge_u32 s4, 0xd000
	s_cselect_b32 s47, 1, 0

.Lw2b34:
	s_lshl_b32 s12, s4, 8
	v_mov_b32_e32 v105, 0
	v_add_u32_e32 v104, s12, v104
	s_nop 0
	v_lshl_add_u64 v[104:105], v[78:79], 0, v[104:105]
	v_fmamk_f32 v21, v40, 0xbdd2d3e8, v100
	v_mul_f32_e32 v21, v8, v21
	v_exp_f32_e32 v21, v21
	v_fmamk_f32 v14, v41, 0xbdd2d3e8, v100
	v_pk_mul_f32 v[6:7], v[6:7], v[28:29]

.Lw2b35:
	v_mul_f32_e32 v14, v9, v14
	v_cvt_pk_f16_f32 v6, v6, v7
	v_add_f32_e32 v7, 1.0, v21
	v_exp_f32_e32 v21, v14
	v_rcp_f32_e32 v28, v7
	v_pk_mul_f32 v[14:15], v[20:21], v[24:25] op_sel_hi:[0,1]
	s_waitcnt lgkmcnt(0)
	v_pk_fma_f32 v[14:15], v[42:43], v[14:15], v[50:51]
	v_add_f32_e32 v7, 1.0, v21
	v_pk_mul_f32 v[24:25], v[14:15], v[14:15]
	v_rcp_f32_e32 v29, v7

.Lw2b36:
	v_fmamk_f32 v24, v24, 0xbdd2d3e8, v100
	v_mul_f32_e32 v24, v14, v24
	v_exp_f32_e32 v24, v24
	v_fmamk_f32 v21, v25, 0xbdd2d3e8, v100
	v_mul_f32_e32 v21, v15, v21
	v_pk_mul_f32 v[8:9], v[8:9], v[28:29]
	v_add_f32_e32 v7, 1.0, v24
	v_pk_mul_f32 v[24:25], v[20:21], v[38:39] op_sel_hi:[0,1]
	v_pk_fma_f32 v[24:25], v[44:45], v[24:25], v[52:53]
	v_exp_f32_e32 v21, v21

.Lw2b37:
	v_pk_mul_f32 v[38:39], v[24:25], v[24:25]
	v_rcp_f32_e32 v40, v7
	v_fmamk_f32 v38, v38, 0xbdd2d3e8, v100
	v_fmamk_f32 v39, v39, 0xbdd2d3e8, v100
	v_mul_f32_e32 v38, v24, v38
	v_mul_f32_e32 v39, v25, v39
	v_exp_f32_e32 v38, v38
	v_exp_f32_e32 v39, v39
	v_add_f32_e32 v7, 1.0, v21
	v_mov_b32_e32 v21, v86
	v_add_f32_e32 v38, 1.0, v38
	v_add_f32_e32 v39, 1.0, v39

.Lw2b38:
	v_rcp_f32_e32 v38, v38
	v_rcp_f32_e32 v39, v39
	v_rcp_f32_e32 v41, v7
	v_pk_mul_f32 v[24:25], v[24:25], v[38:39]
	s_nop 0
	s_nop 0
	v_lshl_add_u32 v7, v21, 2, v102
	v_add_u32_e32 v54, 0x420, v7
	v_add_u32_e32 v48, 0x428, v7
	v_add_u32_e32 v52, 0x430, v7

.Lw2b39:
	ds_read2_b32 v[38:39], v7 offset0:138 offset1:139
	ds_read2_b32 v[42:43], v7 offset0:142 offset1:143
	ds_read2_b32 v[44:45], v7 offset0:140 offset1:141
	ds_read2_b32 v[46:47], v7 offset0:136 offset1:137
	v_add_u32_e32 v7, 0x438, v7
	ds_read2_b32 v[48:49], v48 offset1:1
	ds_read2_b32 v[50:51], v7 offset1:1
	ds_read2_b32 v[52:53], v52 offset1:1

.Lw2b40:
	ds_read2_b32 v[54:55], v54 offset1:1
	v_cvt_pk_f16_f32 v7, v8, v9
	v_pk_mul_f32 v[8:9], v[14:15], v[40:41]
	s_nop 0
	v_cvt_pk_f16_f32 v8, v8, v9
	v_pk_mul_f32 v[14:15], v[20:21], v[36:37] op_sel_hi:[0,1]
	s_waitcnt lgkmcnt(0)
	v_pk_fma_f32 v[14:15], v[46:47], v[14:15], v[54:55]

.Lw2b41:
	v_pk_mul_f32 v[22:23], v[20:21], v[22:23] op_sel_hi:[0,1]
	v_pk_mul_f32 v[28:29], v[14:15], v[14:15]
	v_pk_fma_f32 v[22:23], v[38:39], v[22:23], v[48:49]
	v_fmamk_f32 v9, v28, 0xbdd2d3e8, v100
	v_mul_f32_e32 v9, v14, v9
	v_fmamk_f32 v28, v29, 0xbdd2d3e8, v100
	v_exp_f32_e32 v9, v9
	v_mul_f32_e32 v28, v15, v28
	v_exp_f32_e32 v29, v28
	v_pk_mul_f32 v[36:37], v[22:23], v[22:23]

.Lw2b42:
	v_add_f32_e32 v9, 1.0, v9
	v_rcp_f32_e32 v28, v9
	v_add_f32_e32 v9, 1.0, v29
	v_rcp_f32_e32 v29, v9
	v_fmamk_f32 v9, v36, 0xbdd2d3e8, v100
	v_mul_f32_e32 v9, v22, v9
	v_exp_f32_e32 v36, v9
	v_cvt_pk_f16_f32 v9, v24, v25
	v_fmamk_f32 v24, v37, 0xbdd2d3e8, v100
	v_pk_mul_f32 v[16:17], v[20:21], v[16:17] op_sel_hi:[0,1]

.Lw2b43:
	v_mul_f32_e32 v24, v23, v24
	v_pk_fma_f32 v[16:17], v[44:45], v[16:17], v[52:53]
	v_pk_mul_f32 v[14:15], v[14:15], v[28:29]
	v_exp_f32_e32 v29, v24
	v_pk_mul_f32 v[24:25], v[16:17], v[16:17]
	v_cvt_pk_f16_f32 v14, v14, v15
	v_fmamk_f32 v24, v24, 0xbdd2d3e8, v100
	v_mul_f32_e32 v24, v16, v24
	v_exp_f32_e32 v24, v24
	v_add_f32_e32 v15, 1.0, v36

.Lw2b44:
	v_rcp_f32_e32 v28, v15
	v_add_f32_e32 v15, 1.0, v29
	v_rcp_f32_e32 v29, v15
	v_add_f32_e32 v15, 1.0, v24
	v_fmamk_f32 v24, v25, 0xbdd2d3e8, v100
	v_mul_f32_e32 v36, v17, v24
	v_pk_mul_f32 v[24:25], v[20:21], v[34:35] op_sel_hi:[0,1]
	v_pk_fma_f32 v[24:25], v[42:43], v[24:25], v[50:51]
	v_exp_f32_e32 v37, v36
	v_pk_mul_f32 v[34:35], v[24:25], v[24:25]
	v_rcp_f32_e32 v36, v15

.Lw2b45:
	v_fmamk_f32 v34, v34, 0xbdd2d3e8, v100
	v_fmamk_f32 v35, v35, 0xbdd2d3e8, v100
	v_mul_f32_e32 v34, v24, v34
	v_mul_f32_e32 v35, v25, v35
	v_exp_f32_e32 v34, v34
	v_exp_f32_e32 v35, v35
	v_add_f32_e32 v15, 1.0, v37
	v_rcp_f32_e32 v37, v15
	v_add_f32_e32 v34, 1.0, v34
	v_add_f32_e32 v35, 1.0, v35
	v_rcp_f32_e32 v34, v34
	v_rcp_f32_e32 v35, v35
	v_pk_mul_f32 v[22:23], v[22:23], v[28:29]

.Lw2b46:
	v_pk_mul_f32 v[16:17], v[16:17], v[36:37]
	v_pk_mul_f32 v[24:25], v[24:25], v[34:35]
	s_nop 0
	v_cvt_pk_f16_f32 v16, v16, v17
	v_lshl_add_u32 v15, v21, 2, v102
	v_add_u32_e32 v50, 0x440, v15
	v_add_u32_e32 v44, 0x448, v15
	v_add_u32_e32 v48, 0x450, v15

.Lw2b47:
	ds_read2_b32 v[34:35], v15 offset0:146 offset1:147
	ds_read2_b32 v[38:39], v15 offset0:150 offset1:151
	ds_read2_b32 v[40:41], v15 offset0:148 offset1:149
	ds_read2_b32 v[42:43], v15 offset0:144 offset1:145
	v_add_u32_e32 v15, 0x458, v15
	ds_read2_b32 v[44:45], v44 offset1:1
	ds_read2_b32 v[46:47], v15 offset1:1

.Lw2b48:
	ds_read2_b32 v[48:49], v48 offset1:1
	ds_read2_b32 v[50:51], v50 offset1:1
	v_cvt_pk_f16_f32 v15, v22, v23
	v_pk_mul_f32 v[12:13], v[20:21], v[12:13] op_sel_hi:[0,1]
	s_waitcnt lgkmcnt(0)
	v_pk_fma_f32 v[12:13], v[42:43], v[12:13], v[50:51]
	v_pk_mul_f32 v[28:29], v[20:21], v[30:31] op_sel_hi:[0,1]
	v_pk_mul_f32 v[22:23], v[12:13], v[12:13]

.Lw2b49:
	v_pk_fma_f32 v[28:29], v[34:35], v[28:29], v[44:45]
	v_fmamk_f32 v17, v22, 0xbdd2d3e8, v100
	v_mul_f32_e32 v17, v12, v17
	v_fmamk_f32 v22, v23, 0xbdd2d3e8, v100
	v_exp_f32_e32 v17, v17
	v_mul_f32_e32 v22, v13, v22
	v_exp_f32_e32 v23, v22
	v_pk_mul_f32 v[30:31], v[28:29], v[28:29]
	v_add_f32_e32 v17, 1.0, v17
	v_rcp_f32_e32 v22, v17
	v_add_f32_e32 v17, 1.0, v23

.Lw2b50:
	v_rcp_f32_e32 v23, v17
	v_fmamk_f32 v17, v30, 0xbdd2d3e8, v100
	v_mul_f32_e32 v17, v28, v17
	v_exp_f32_e32 v30, v17
	v_pk_mul_f32 v[12:13], v[12:13], v[22:23]
	v_cvt_pk_f16_f32 v17, v24, v25
	v_cvt_pk_f16_f32 v22, v12, v13
	v_fmamk_f32 v12, v31, 0xbdd2d3e8, v100
	v_mul_f32_e32 v12, v29, v12
	v_exp_f32_e32 v31, v12

.Lw2b51:
	v_pk_mul_f32 v[12:13], v[20:21], v[32:33] op_sel_hi:[0,1]
	v_pk_fma_f32 v[12:13], v[40:41], v[12:13], v[48:49]
	v_add_f32_e32 v23, 1.0, v30
	v_pk_mul_f32 v[24:25], v[12:13], v[12:13]
	v_rcp_f32_e32 v30, v23
	v_fmamk_f32 v24, v24, 0xbdd2d3e8, v100
	v_mul_f32_e32 v24, v12, v24
	v_exp_f32_e32 v24, v24
	v_add_f32_e32 v23, 1.0, v31
	v_pk_mul_f32 v[10:11], v[20:21], v[10:11] op_sel_hi:[0,1]

.Lw2b52:
	v_rcp_f32_e32 v31, v23
	v_add_f32_e32 v23, 1.0, v24
	v_fmamk_f32 v24, v25, 0xbdd2d3e8, v100
	v_pk_fma_f32 v[10:11], v[38:39], v[10:11], v[46:47]
	v_mul_f32_e32 v32, v13, v24
	v_pk_mul_f32 v[24:25], v[10:11], v[10:11]
	v_exp_f32_e32 v33, v32
	v_fmamk_f32 v24, v24, 0xbdd2d3e8, v100
	v_fmamk_f32 v25, v25, 0xbdd2d3e8, v100
	v_mul_f32_e32 v24, v10, v24

.Lw2b53:
	v_mul_f32_e32 v25, v11, v25
	v_exp_f32_e32 v24, v24
	v_exp_f32_e32 v25, v25
	v_rcp_f32_e32 v32, v23
	v_add_f32_e32 v23, 1.0, v33
	v_add_f32_e32 v24, 1.0, v24
	v_add_f32_e32 v25, 1.0, v25
	v_rcp_f32_e32 v24, v24
	v_rcp_f32_e32 v25, v25
	v_rcp_f32_e32 v33, v23
	v_pk_mul_f32 v[10:11], v[10:11], v[24:25]
	s_nop 0
	v_pk_mul_f32 v[12:13], v[12:13], v[32:33]

.Lw2b54:
	v_lshl_add_u32 v21, v21, 2, v102
	v_add_u32_e32 v24, 0x468, v21
	ds_read2_b32 v[34:35], v21 offset0:154 offset1:155
	ds_read2_b32 v[36:37], v21 offset0:158 offset1:159
	ds_read2_b32 v[38:39], v21 offset0:156 offset1:157
	ds_read2_b32 v[40:41], v21 offset0:152 offset1:153
	v_add_u32_e32 v23, 0x460, v21
	v_add_u32_e32 v25, 0x470, v21

.Lw2b55:
	v_add_u32_e32 v21, 0x478, v21
	ds_read2_b32 v[42:43], v24 offset1:1
	ds_read2_b32 v[44:45], v21 offset1:1
	ds_read2_b32 v[46:47], v25 offset1:1
	ds_read2_b32 v[48:49], v23 offset1:1
	v_pk_mul_f32 v[24:25], v[28:29], v[30:31]
	s_nop 0
	v_cvt_pk_f16_f32 v23, v24, v25

.Lw2b56:
	v_cvt_pk_f16_f32 v24, v12, v13
	v_pk_mul_f32 v[4:5], v[20:21], v[4:5] op_sel_hi:[0,1]
	s_waitcnt lgkmcnt(0)
	v_pk_fma_f32 v[4:5], v[40:41], v[4:5], v[48:49]
	ds_write_b128 v125, v[6:9]
	v_pk_mul_f32 v[12:13], v[4:5], v[4:5]
	v_pk_mul_f32 v[0:1], v[20:21], v[0:1] op_sel_hi:[0,1]
	v_fmamk_f32 v12, v12, 0xbdd2d3e8, v100

.Lw2b57:
	v_fmamk_f32 v13, v13, 0xbdd2d3e8, v100
	v_mul_f32_e32 v12, v4, v12
	v_mul_f32_e32 v13, v5, v13
	v_exp_f32_e32 v12, v12
	v_exp_f32_e32 v13, v13
	v_pk_fma_f32 v[0:1], v[38:39], v[0:1], v[46:47]
	v_cvt_pk_f16_f32 v25, v10, v11
	v_add_f32_e32 v6, 1.0, v12
	v_add_f32_e32 v7, 1.0, v13
	v_rcp_f32_e32 v6, v6
	v_rcp_f32_e32 v7, v7

.Lw2b58:
	v_pk_mul_f32 v[10:11], v[0:1], v[0:1]
	v_pk_mul_f32 v[2:3], v[20:21], v[2:3] op_sel_hi:[0,1]
	v_pk_fma_f32 v[2:3], v[36:37], v[2:3], v[44:45]
	v_pk_mul_f32 v[4:5], v[4:5], v[6:7]
	v_pk_mul_f32 v[6:7], v[20:21], v[18:19] op_sel_hi:[0,1]
	v_pk_fma_f32 v[6:7], v[34:35], v[6:7], v[42:43]
	v_cvt_pk_f16_f32 v4, v4, v5
	v_pk_mul_f32 v[8:9], v[6:7], v[6:7]

.Lw2b59:
	s_mov_b64 s[4:5], 0
	v_fmamk_f32 v8, v8, 0xbdd2d3e8, v100
	v_mul_f32_e32 v8, v6, v8
	v_fmamk_f32 v9, v9, 0xbdd2d3e8, v100
	v_exp_f32_e32 v8, v8
	v_mul_f32_e32 v9, v7, v9
	v_exp_f32_e32 v9, v9
	ds_write_b128 v125, v[14:17] offset:16
	v_add_f32_e32 v5, 1.0, v8
	v_rcp_f32_e32 v8, v5
	v_add_f32_e32 v5, 1.0, v9

.Lw2b60:
	v_rcp_f32_e32 v9, v5
	v_fmamk_f32 v5, v10, 0xbdd2d3e8, v100
	v_mul_f32_e32 v5, v0, v5
	v_fmamk_f32 v10, v11, 0xbdd2d3e8, v100
	v_exp_f32_e32 v5, v5
	v_mul_f32_e32 v10, v1, v10
	v_exp_f32_e32 v10, v10
	v_pk_mul_f32 v[6:7], v[6:7], v[8:9]
	v_add_f32_e32 v5, 1.0, v5
	v_rcp_f32_e32 v8, v5
	v_add_f32_e32 v5, 1.0, v10
	v_pk_mul_f32 v[10:11], v[2:3], v[2:3]

.Lw2b61:
	ds_write_b128 v125, v[22:25] offset:32
	v_fmamk_f32 v9, v10, 0xbdd2d3e8, v100
	v_mul_f32_e32 v9, v2, v9
	v_exp_f32_e32 v10, v9
	v_fmamk_f32 v9, v11, 0xbdd2d3e8, v100
	v_mul_f32_e32 v9, v3, v9
	v_exp_f32_e32 v11, v9
	v_rcp_f32_e32 v9, v5
	v_add_f32_e32 v5, 1.0, v10
	v_rcp_f32_e32 v10, v5
	v_add_f32_e32 v5, 1.0, v11

.Lw2b62:
	v_rcp_f32_e32 v11, v5
	v_pk_mul_f32 v[0:1], v[0:1], v[8:9]
	v_cvt_pk_f16_f32 v5, v6, v7
	v_cvt_pk_f16_f32 v6, v0, v1
	v_pk_mul_f32 v[0:1], v[2:3], v[10:11]
	s_nop 0
	v_cvt_pk_f16_f32 v7, v0, v1
	ds_write_b128 v125, v[4:7] offset:48
	ds_read_b128 v[4:7], v126

.Lw2b63:
	ds_read_b128 v[8:11], v126 offset:1088
	ds_read_b128 v[12:15], v126 offset:2176
	ds_read_b128 v[16:19], v126 offset:3264
	s_cmp_lg_u32 s47, 0
	s_waitcnt lgkmcnt(0)
	s_cbranch_scc1 .Lh1_wt
	global_store_dwordx4 v[104:105], v[4:7], off
	global_store_dwordx4 v[104:105], v[8:11], off offset:1024
	global_store_dwordx4 v[104:105], v[12:15], off offset:2048

.Lw2b64:
	global_store_dwordx4 v[104:105], v[16:19], off offset:3072
	s_branch .LBB2_8
.Lh1_wt:
	global_store_dwordx4 v[104:105], v[4:7], off sc1
	global_store_dwordx4 v[104:105], v[8:11], off offset:1024 sc1
	global_store_dwordx4 v[104:105], v[12:15], off offset:2048 sc1
	global_store_dwordx4 v[104:105], v[16:19], off offset:3072 sc1

.LBB2_9:
	v_mov_b32_e32 v0, 0
.Lw2t65:
	s_cbranch_execz .Lw2c65
.Lw2b65:
	s_and_saveexec_b64 s[4:5], s[0:1]
	s_cbranch_execz .LBB2_13
	s_mov_b64 s[14:15], exec
	v_mbcnt_lo_u32_b32 v0, s14, 0
	v_mbcnt_hi_u32_b32 v0, s15, v0
	v_cmp_eq_u32_e32 vcc, 0, v0
	s_and_saveexec_b64 s[10:11], vcc
	s_bcnt1_i32_b64 s12, s[14:15]
	v_mov_b32_e32 v1, s12
	ds_add_rtn_u32 v1, v96, v1
	s_or_b64 exec, exec, s[10:11]
	s_waitcnt lgkmcnt(0)

.Lw2b66:
	v_readfirstlane_b32 s10, v1
	s_nop 1
	v_add_u32_e32 v0, s10, v0
.LBB2_13:
	s_or_b64 exec, exec, s[4:5]
	v_readfirstlane_b32 s4, v0
	s_waitcnt lgkmcnt(0)
	s_mul_i32 s10, s4, s3
	s_add_i32 s10, s10, s2
	s_cmpk_gt_i32 s10, 0x1869
	s_mov_b64 s[4:5], -1
	s_cbranch_scc1 .LBB2_8
	ds_read_b128 v[28:31], v97
	ds_read_b128 v[24:27], v97 offset:16

.Lw2b67:
	ds_read_b128 v[20:23], v97 offset:32
	ds_read_b128 v[16:19], v97 offset:48
	ds_read_b128 v[12:15], v97 offset:64
	ds_read_b128 v[8:11], v97 offset:80
	ds_read_b128 v[4:7], v97 offset:96
	ds_read_b128 v[0:3], v97 offset:112
	s_lshl_b32 s4, s10, 4
	s_ashr_i32 s5, s4, 31
	v_lshl_add_u64 v[80:81], s[4:5], 2, v[74:75]

.Lw2b68:
	s_mov_b32 s5, 0
	s_mov_b64 s[18:19], -1
	s_branch .LBB2_16
.LBB2_15:
	s_or_b64 exec, exec, s[14:15]
	v_mov_b32_e32 v48, v77
	ds_read_b128 v[32:35], v98
	ds_read_b128 v[36:39], v98 offset:64
	ds_read_b128 v[40:43], v98 offset:128
	ds_read_b128 v[44:47], v98 offset:192
	s_nop 0

.Lw2b69:
	v_lshlrev_b32_e32 v48, 4, v48
	v_lshl_add_u32 v103, s5, 15, v48
	ds_read_b128 v[48:51], v103
	ds_read_b128 v[52:55], v103 offset:1024
	ds_read_b128 v[56:59], v103 offset:2048
	ds_read_b128 v[60:63], v103 offset:3072
	ds_read_b128 v[64:67], v103 offset:4096
	ds_read_b128 v[68:71], v103 offset:5120

.Lw2b70:
	ds_read_b128 v[104:107], v103 offset:6144
	ds_read_b128 v[108:111], v103 offset:7168
	s_waitcnt lgkmcnt(7)
	v_mfma_f32_16x16x32_f16 v[28:31], v[48:51], v[32:35], v[28:31]
	s_waitcnt lgkmcnt(6)
	v_mfma_f32_16x16x32_f16 v[24:27], v[52:55], v[32:35], v[24:27]
	s_waitcnt lgkmcnt(5)
	v_mfma_f32_16x16x32_f16 v[20:23], v[56:59], v[32:35], v[20:23]
	s_waitcnt lgkmcnt(4)
	v_mfma_f32_16x16x32_f16 v[16:19], v[60:63], v[32:35], v[16:19]

.Lw2b71:
	ds_read_b128 v[48:51], v103 offset:8192
	ds_read_b128 v[52:55], v103 offset:9216
	ds_read_b128 v[56:59], v103 offset:10240
	ds_read_b128 v[60:63], v103 offset:11264
	s_waitcnt lgkmcnt(7)
	v_mfma_f32_16x16x32_f16 v[12:15], v[64:67], v[32:35], v[12:15]
	s_waitcnt lgkmcnt(6)
	v_mfma_f32_16x16x32_f16 v[8:11], v[68:71], v[32:35], v[8:11]

.Lw2b72:
	s_waitcnt lgkmcnt(5)
	v_mfma_f32_16x16x32_f16 v[4:7], v[104:107], v[32:35], v[4:7]
	s_waitcnt lgkmcnt(4)
	v_mfma_f32_16x16x32_f16 v[0:3], v[108:111], v[32:35], v[0:3]
	ds_read_b128 v[32:35], v103 offset:12288
	ds_read_b128 v[64:67], v103 offset:13312
	ds_read_b128 v[68:71], v103 offset:14336
	ds_read_b128 v[104:107], v103 offset:15360
	s_waitcnt lgkmcnt(7)

.Lw2b73:
	v_mfma_f32_16x16x32_f16 v[28:31], v[48:51], v[36:39], v[28:31]
	s_waitcnt lgkmcnt(6)
	v_mfma_f32_16x16x32_f16 v[24:27], v[52:55], v[36:39], v[24:27]
	s_waitcnt lgkmcnt(5)
	v_mfma_f32_16x16x32_f16 v[20:23], v[56:59], v[36:39], v[20:23]
	s_waitcnt lgkmcnt(4)
	v_mfma_f32_16x16x32_f16 v[16:19], v[60:63], v[36:39], v[16:19]
	ds_read_b128 v[48:51], v103 offset:16384
	ds_read_b128 v[52:55], v103 offset:17408

.Lw2b74:
	ds_read_b128 v[56:59], v103 offset:18432
	ds_read_b128 v[60:63], v103 offset:19456
	s_waitcnt lgkmcnt(7)
	v_mfma_f32_16x16x32_f16 v[12:15], v[32:35], v[36:39], v[12:15]
	s_waitcnt lgkmcnt(6)
	v_mfma_f32_16x16x32_f16 v[8:11], v[64:67], v[36:39], v[8:11]
	s_waitcnt lgkmcnt(5)
	v_mfma_f32_16x16x32_f16 v[4:7], v[68:71], v[36:39], v[4:7]
	s_waitcnt lgkmcnt(4)
	v_mfma_f32_16x16x32_f16 v[0:3], v[104:107], v[36:39], v[0:3]

.Lw2b75:
	ds_read_b128 v[32:35], v103 offset:20480
	ds_read_b128 v[36:39], v103 offset:21504
	ds_read_b128 v[64:67], v103 offset:22528
	ds_read_b128 v[68:71], v103 offset:23552
	s_waitcnt lgkmcnt(7)
	v_mfma_f32_16x16x32_f16 v[28:31], v[48:51], v[40:43], v[28:31]
	s_waitcnt lgkmcnt(6)
	v_mfma_f32_16x16x32_f16 v[24:27], v[52:55], v[40:43], v[24:27]

.Lw2b76:
	s_waitcnt lgkmcnt(5)
	v_mfma_f32_16x16x32_f16 v[20:23], v[56:59], v[40:43], v[20:23]
	s_waitcnt lgkmcnt(4)
	v_mfma_f32_16x16x32_f16 v[16:19], v[60:63], v[40:43], v[16:19]
	ds_read_b128 v[48:51], v103 offset:24576
	ds_read_b128 v[52:55], v103 offset:25600
	ds_read_b128 v[56:59], v103 offset:26624
	ds_read_b128 v[60:63], v103 offset:27648
	s_waitcnt lgkmcnt(7)

.Lw2b77:
	v_mfma_f32_16x16x32_f16 v[12:15], v[32:35], v[40:43], v[12:15]
	s_waitcnt lgkmcnt(6)
	v_mfma_f32_16x16x32_f16 v[8:11], v[36:39], v[40:43], v[8:11]
	s_waitcnt lgkmcnt(5)
	v_mfma_f32_16x16x32_f16 v[4:7], v[64:67], v[40:43], v[4:7]
	s_waitcnt lgkmcnt(4)
	v_mfma_f32_16x16x32_f16 v[0:3], v[68:71], v[40:43], v[0:3]
	ds_read_b128 v[32:35], v103 offset:28672
	ds_read_b128 v[36:39], v103 offset:29696

.Lw2b78:
	ds_read_b128 v[40:43], v103 offset:30720
	ds_read_b128 v[64:67], v103 offset:31744
	s_waitcnt lgkmcnt(7)
	v_mfma_f32_16x16x32_f16 v[28:31], v[48:51], v[44:47], v[28:31]
	s_waitcnt lgkmcnt(6)
	v_mfma_f32_16x16x32_f16 v[24:27], v[52:55], v[44:47], v[24:27]
	s_waitcnt lgkmcnt(5)
	v_mfma_f32_16x16x32_f16 v[20:23], v[56:59], v[44:47], v[20:23]
	s_waitcnt lgkmcnt(4)
	v_mfma_f32_16x16x32_f16 v[16:19], v[60:63], v[44:47], v[16:19]

.Lw2b79:
	s_waitcnt lgkmcnt(3)
	v_mfma_f32_16x16x32_f16 v[12:15], v[32:35], v[44:47], v[12:15]
	s_waitcnt lgkmcnt(2)
	v_mfma_f32_16x16x32_f16 v[8:11], v[36:39], v[44:47], v[8:11]
	s_waitcnt lgkmcnt(1)
	v_mfma_f32_16x16x32_f16 v[4:7], v[40:43], v[44:47], v[4:7]
	s_waitcnt lgkmcnt(0)
	v_mfma_f32_16x16x32_f16 v[0:3], v[64:67], v[44:47], v[0:3]
	s_mov_b32 s5, 1
	s_mov_b64 s[18:19], 0

.LBB2_16:
	s_mul_i32 s12, s5, 0x186a1
	v_lshl_add_u64 v[32:33], s[12:13], 2, v[80:81]
	global_load_dword v113, v[32:33], off
	global_load_dword v103, v[32:33], off offset:16
	s_mov_b32 s14, s13
	s_mov_b32 s15, s13
	s_mul_i32 s12, s5, 0xc3500
	s_lshl_b64 s[10:11], s[12:13], 2

.Lw2b81:
	s_mov_b32 s12, s13
	v_mov_b64_e32 v[34:35], s[14:15]
	v_mov_b64_e32 v[32:33], s[12:13]
	s_add_u32 s16, s6, s10
	ds_write_b128 v85, v[32:35]
	ds_write_b128 v85, v[32:35] offset:16
	ds_write_b128 v85, v[32:35] offset:32
	ds_write_b128 v85, v[32:35] offset:48
	s_addc_u32 s17, s7, s11
	v_mov_b32_e32 v116, 0x3f86a0

.Lw2b82:
	s_waitcnt vmcnt(1)
	v_add_u32_e32 v32, v113, v82
	s_waitcnt vmcnt(0)
	v_cmp_lt_i32_e32 vcc, v32, v103
	s_and_saveexec_b64 s[10:11], vcc
	s_cbranch_execz .LBB2_18
	v_ashrrev_i32_e32 v33, 31, v32
	v_lshl_add_u64 v[32:33], v[32:33], 2, s[16:17]
	global_load_dword v116, v[32:33], off
.LBB2_18:
	s_or_b64 exec, exec, s[10:11]
	v_mov_b32_e32 v56, 0
	s_xor_b64 s[10:11], s[18:19], -1
	v_mov_b32_e32 v115, 31
.Lw2t83:
	s_cbranch_execz .Lw2c83
.Lw2b83:
	v_mov_b32_e32 v57, v56
	v_mov_b32_e32 v58, v56
	v_mov_b32_e32 v59, v56
	v_mov_b32_e32 v60, v56
	v_mov_b32_e32 v61, v56
	v_mov_b32_e32 v62, v56
	v_mov_b32_e32 v63, v56
	s_branch .LBB2_20
.LBB2_19:
	s_waitcnt vmcnt(0)
	v_mov_b32_e32 v116, v114
	s_cbranch_execnz .LBB2_90
.LBB2_20:
	s_nop 2
	v_mov_b32_e32 v104, v63
	v_mov_b32_e32 v106, v62
	v_mov_b32_e32 v105, v61
.Lw2t84:
	s_cbranch_execz .Lw2c84
.Lw2b84:
	v_mov_b32_e32 v108, v60
	v_mov_b32_e32 v109, v59
	v_mov_b32_e32 v111, v58
	v_mov_b32_e32 v110, v57
	v_mov_b32_e32 v112, v56
	v_mov_b32_e32 v107, v115
	v_cmp_lt_i32_e32 vcc, v113, v103
	s_cbranch_vccz .LBB2_19
	v_or_b32_e32 v32, 4, v84
	s_waitcnt vmcnt(0)
	ds_bpermute_b32 v66, v84, v116
	ds_bpermute_b32 v123, v32, v116
	v_or_b32_e32 v32, 8, v84

.Lw2b85:
	v_or_b32_e32 v34, 12, v84
	ds_bpermute_b32 v122, v32, v116
	ds_bpermute_b32 v121, v34, v116
	v_or_b32_e32 v34, 16, v84
	ds_bpermute_b32 v120, v34, v116
	v_or_b32_e32 v34, 20, v84
	ds_bpermute_b32 v119, v34, v116
	s_waitcnt lgkmcnt(5)
	v_lshlrev_b32_e32 v32, 8, v66
	s_waitcnt lgkmcnt(4)
	v_lshlrev_b32_e32 v33, 8, v123

.Lw2b86:
	v_or_b32_e32 v34, 24, v84
	v_and_or_b32 v32, v32, s21, v83
	v_and_or_b32 v33, v33, s21, v83
	ds_bpermute_b32 v118, v34, v116
	ds_bpermute_b32 v117, v87, v116
	global_load_dwordx4 v[60:63], v32, s[8:9]
	global_load_dwordx4 v[56:59], v33, s[8:9]
	s_waitcnt lgkmcnt(5)
	v_lshlrev_b32_e32 v32, 8, v122

.Lw2b87:
	s_waitcnt lgkmcnt(4)
	v_lshlrev_b32_e32 v33, 8, v121
	v_and_or_b32 v32, v32, s21, v83
	v_and_or_b32 v33, v33, s21, v83
	global_load_dwordx4 v[52:55], v32, s[8:9]
	global_load_dwordx4 v[48:51], v33, s[8:9]
	s_waitcnt lgkmcnt(3)
	v_lshlrev_b32_e32 v32, 8, v120
	s_waitcnt lgkmcnt(2)
	v_lshlrev_b32_e32 v33, 8, v119
	v_and_or_b32 v32, v32, s21, v83

.Lw2b88:
	v_and_or_b32 v33, v33, s21, v83
	global_load_dwordx4 v[44:47], v32, s[8:9]
	global_load_dwordx4 v[40:43], v33, s[8:9]
	s_waitcnt lgkmcnt(1)
	v_lshlrev_b32_e32 v32, 8, v118
	s_waitcnt lgkmcnt(0)
	v_lshlrev_b32_e32 v33, 8, v117
	v_and_or_b32 v32, v32, s21, v83
	v_and_or_b32 v33, v33, s21, v83

.Lw2b89:
	global_load_dwordx4 v[36:39], v32, s[8:9]
	s_nop 0
	global_load_dwordx4 v[32:35], v33, s[8:9]
	v_or_b32_e32 v64, 16, v82
	v_add_u32_e32 v64, v64, v113
	v_cmp_lt_i32_e32 vcc, v64, v103
	v_mov_b32_e32 v114, 0x3f86a0
	s_and_saveexec_b64 s[14:15], vcc
	s_cbranch_execz .LBB2_23
	v_ashrrev_i32_e32 v65, 31, v64
	v_lshl_add_u64 v[64:65], v[64:65], 2, s[16:17]

.LBB2_23:
	s_or_b64 exec, exec, s[14:15]
	v_ashrrev_i32_e32 v124, 17, v66
	v_cmp_ne_u32_e32 vcc, v124, v107
	s_cmp_lg_u64 vcc, 0
	s_cselect_b64 s[14:15], -1, 0
	s_and_b64 s[18:19], s[14:15], vcc
	v_mov_b32_e32 v115, v107
	v_mov_b32_e32 v68, v112
	v_mov_b32_e32 v69, v110
	v_mov_b32_e32 v70, v111
	v_mov_b32_e32 v71, v109
	v_mov_b32_e32 v64, v108
	v_mov_b32_e32 v65, v105

.Lw2b91:
	v_mov_b32_e32 v66, v106
	v_mov_b32_e32 v67, v104
	s_and_saveexec_b64 s[14:15], s[18:19]
	s_cbranch_execz .LBB2_27
	v_cmp_gt_i32_e32 vcc, 16, v107
	s_and_saveexec_b64 s[18:19], vcc
	s_cbranch_execz .LBB2_26
	v_cvt_pk_f16_f32 v67, v111, v109
	v_cvt_pk_f16_f32 v66, v112, v110
	v_cvt_pk_f16_f32 v65, v106, v104
	v_cvt_pk_f16_f32 v64, v108, v105

.Lw2b92:
	v_mad_u64_u32 v[68:69], s[24:25], v107, s20, v[76:77]
	ds_write_b128 v68, v[64:67]

.Lw2b93:
	v_ashrrev_i32_e32 v123, 17, v123
	s_waitcnt vmcnt(7)
	v_mfma_f32_16x16x16_f16 v[64:67], v[72:73], v[60:61], v[64:67]
	v_cmp_ne_u32_e32 vcc, v123, v115
	s_cmp_lg_u64 vcc, 0
	s_cselect_b64 s[14:15], -1, 0
	v_mfma_f32_16x16x16_f16 v[60:63], v[72:73], v[62:63], v[68:71]
	s_and_b64 s[18:19], s[14:15], vcc
	s_and_saveexec_b64 s[14:15], s[18:19]
	s_cbranch_execz .LBB2_31
	v_cmp_gt_i32_e32 vcc, 16, v115
	s_and_saveexec_b64 s[18:19], vcc
	s_cbranch_execz .LBB2_30

.Lw2b94:
	s_nop 1
	v_cvt_pk_f16_f32 v63, v62, v63
	v_cvt_pk_f16_f32 v62, v60, v61
	v_cvt_pk_f16_f32 v61, v66, v67
	v_cvt_pk_f16_f32 v60, v64, v65
	v_mad_u64_u32 v[64:65], s[24:25], v115, s20, v[76:77]
	ds_write_b128 v64, v[60:63]

.Lw2b95:
	v_mov_b32_e32 v60, 0
	v_mov_b32_e32 v115, v123
	v_mov_b32_e32 v61, v60
	v_mov_b32_e32 v62, v60
	v_mov_b32_e32 v63, v60
	v_mov_b32_e32 v64, v60
	v_mov_b32_e32 v65, v60
	v_mov_b32_e32 v66, v60
	v_mov_b32_e32 v67, v60
.LBB2_31:
	s_or_b64 exec, exec, s[14:15]
	v_ashrrev_i32_e32 v68, 17, v122
	s_waitcnt vmcnt(6)
	v_mfma_f32_16x16x16_f16 v[64:67], v[72:73], v[56:57], v[64:67]
	v_cmp_ne_u32_e32 vcc, v68, v115

.Lw2b96:
	s_cmp_lg_u64 vcc, 0
	s_cselect_b64 s[14:15], -1, 0
	v_mfma_f32_16x16x16_f16 v[56:59], v[72:73], v[58:59], v[60:63]
	s_and_b64 s[18:19], s[14:15], vcc
	s_and_saveexec_b64 s[14:15], s[18:19]
	s_cbranch_execz .LBB2_35
	v_cmp_gt_i32_e32 vcc, 16, v115
	s_and_saveexec_b64 s[18:19], vcc
	s_cbranch_execz .LBB2_34
	s_nop 1
	v_cvt_pk_f16_f32 v59, v58, v59
	v_cvt_pk_f16_f32 v58, v56, v57

.Lw2b97:
	v_cvt_pk_f16_f32 v57, v66, v67
	v_cvt_pk_f16_f32 v56, v64, v65
	v_mad_u64_u32 v[60:61], s[24:25], v115, s20, v[76:77]
	ds_write_b128 v60, v[56:59]

.Lw2b98:
	v_mov_b32_e32 v64, v56
	v_mov_b32_e32 v65, v56
	v_mov_b32_e32 v66, v56
	v_mov_b32_e32 v67, v56
.LBB2_35:
	s_or_b64 exec, exec, s[14:15]
	v_ashrrev_i32_e32 v68, 17, v121
	s_waitcnt vmcnt(5)
	v_mfma_f32_16x16x16_f16 v[60:63], v[72:73], v[52:53], v[64:67]
	v_cmp_ne_u32_e32 vcc, v68, v115
	s_cmp_lg_u64 vcc, 0
	s_cselect_b64 s[14:15], -1, 0
	v_mfma_f32_16x16x16_f16 v[52:55], v[72:73], v[54:55], v[56:59]
	s_and_b64 s[18:19], s[14:15], vcc

.Lw2b101:
	v_ashrrev_i32_e32 v64, 17, v120
	s_waitcnt vmcnt(4)
	v_mfma_f32_16x16x16_f16 v[56:59], v[72:73], v[48:49], v[60:63]
	v_cmp_ne_u32_e32 vcc, v64, v115
	s_cmp_lg_u64 vcc, 0
	s_cselect_b64 s[14:15], -1, 0
	v_mfma_f32_16x16x16_f16 v[48:51], v[72:73], v[50:51], v[52:55]
	s_and_b64 s[18:19], s[14:15], vcc
	s_and_saveexec_b64 s[14:15], s[18:19]
	s_cbranch_execz .LBB2_43
	v_cmp_gt_i32_e32 vcc, 16, v115
	s_and_saveexec_b64 s[18:19], vcc
	s_cbranch_execz .LBB2_42

.LBB2_43:
	s_or_b64 exec, exec, s[14:15]
	v_ashrrev_i32_e32 v60, 17, v119
	s_waitcnt vmcnt(3)
	v_mfma_f32_16x16x16_f16 v[52:55], v[72:73], v[44:45], v[56:59]
	v_cmp_ne_u32_e32 vcc, v60, v115

.LBB2_47:
	s_or_b64 exec, exec, s[14:15]
	v_ashrrev_i32_e32 v56, 17, v118
	s_waitcnt vmcnt(2)
	v_mfma_f32_16x16x16_f16 v[48:51], v[72:73], v[40:41], v[52:55]
	v_cmp_ne_u32_e32 vcc, v56, v115
	s_cmp_lg_u64 vcc, 0
	s_cselect_b64 s[14:15], -1, 0
	v_mfma_f32_16x16x16_f16 v[40:43], v[72:73], v[42:43], v[44:47]
	s_and_b64 s[18:19], s[14:15], vcc

.Lw2b109:
	v_ashrrev_i32_e32 v52, 17, v117
	s_waitcnt vmcnt(1)
	v_mfma_f32_16x16x16_f16 v[44:47], v[72:73], v[36:37], v[48:51]
	v_cmp_ne_u32_e32 vcc, v52, v115
	s_cmp_lg_u64 vcc, 0
	s_cselect_b64 s[14:15], -1, 0
	v_mfma_f32_16x16x16_f16 v[36:39], v[72:73], v[38:39], v[40:43]
	s_and_b64 s[18:19], s[14:15], vcc
	s_and_saveexec_b64 s[14:15], s[18:19]
	s_cbranch_execz .LBB2_55
	v_cmp_gt_i32_e32 vcc, 16, v115
	s_and_saveexec_b64 s[18:19], vcc
	s_cbranch_execz .LBB2_54

.LBB2_55:
	s_or_b64 exec, exec, s[14:15]
	s_waitcnt vmcnt(0)
	v_mfma_f32_16x16x16_f16 v[60:63], v[72:73], v[32:33], v[44:47]
	v_add_u32_e32 v32, 8, v113
	v_cmp_lt_i32_e32 vcc, v32, v103

.Lw2b112:
	v_mfma_f32_16x16x16_f16 v[56:59], v[72:73], v[34:35], v[36:39]
	s_cbranch_vccz .LBB2_89
	ds_bpermute_b32 v123, v88, v116
	ds_bpermute_b32 v122, v89, v116
	ds_bpermute_b32 v121, v90, v116
	ds_bpermute_b32 v120, v91, v116
	ds_bpermute_b32 v119, v92, v116
	ds_bpermute_b32 v118, v93, v116

.Lw2b113:
	s_waitcnt lgkmcnt(5)
	v_lshlrev_b32_e32 v32, 8, v123
	s_waitcnt lgkmcnt(4)
	v_lshlrev_b32_e32 v33, 8, v122
	v_and_or_b32 v32, v32, s21, v83
	v_and_or_b32 v33, v33, s21, v83
	ds_bpermute_b32 v117, v94, v116
	ds_bpermute_b32 v116, v95, v116
	global_load_dwordx4 v[68:71], v32, s[8:9]
	global_load_dwordx4 v[64:67], v33, s[8:9]

.Lw2b114:
	s_waitcnt lgkmcnt(5)
	v_lshlrev_b32_e32 v32, 8, v121
	s_waitcnt lgkmcnt(4)
	v_lshlrev_b32_e32 v33, 8, v120
	v_and_or_b32 v32, v32, s21, v83
	v_and_or_b32 v33, v33, s21, v83
	global_load_dwordx4 v[52:55], v32, s[8:9]
	global_load_dwordx4 v[48:51], v33, s[8:9]
	s_waitcnt lgkmcnt(3)
	v_lshlrev_b32_e32 v32, 8, v119

.Lw2b115:
	s_waitcnt lgkmcnt(2)
	v_lshlrev_b32_e32 v33, 8, v118
	v_and_or_b32 v32, v32, s21, v83
	v_and_or_b32 v33, v33, s21, v83
	global_load_dwordx4 v[44:47], v32, s[8:9]
	global_load_dwordx4 v[40:43], v33, s[8:9]
	s_waitcnt lgkmcnt(1)
	v_lshlrev_b32_e32 v32, 8, v117
	s_waitcnt lgkmcnt(0)
	v_lshlrev_b32_e32 v33, 8, v116
	v_and_or_b32 v32, v32, s21, v83

.Lw2b116:
	v_and_or_b32 v33, v33, s21, v83
	global_load_dwordx4 v[36:39], v32, s[8:9]
	s_nop 0
	global_load_dwordx4 v[32:35], v33, s[8:9]
	v_ashrrev_i32_e32 v123, 17, v123
	v_cmp_ne_u32_e32 vcc, v123, v115
	s_cmp_lg_u64 vcc, 0
	s_cselect_b64 s[14:15], -1, 0
	s_and_b64 s[18:19], s[14:15], vcc
	s_and_saveexec_b64 s[14:15], s[18:19]
	s_cbranch_execz .LBB2_60

.Lw2b117:
	v_cmp_gt_i32_e32 vcc, 16, v115
	s_and_saveexec_b64 s[18:19], vcc
	s_cbranch_execz .LBB2_59
	v_cvt_pk_f16_f32 v59, v58, v59
	v_cvt_pk_f16_f32 v58, v56, v57
	v_cvt_pk_f16_f32 v57, v62, v63
	v_cvt_pk_f16_f32 v56, v60, v61
	v_mad_u64_u32 v[60:61], s[24:25], v115, s20, v[76:77]
	ds_write_b128 v60, v[56:59]
.LBB2_59:
.Lw2t118:
	s_cbranch_execz .Lw2c118
.Lw2b118:
	s_or_b64 exec, exec, s[18:19]
	v_mov_b32_e32 v56, 0
	v_mov_b32_e32 v115, v123
	v_mov_b32_e32 v57, v56
	v_mov_b32_e32 v58, v56
	v_mov_b32_e32 v59, v56
	v_mov_b32_e32 v60, v56
	v_mov_b32_e32 v61, v56
	v_mov_b32_e32 v62, v56
	v_mov_b32_e32 v63, v56
.LBB2_60:
	s_or_b64 exec, exec, s[14:15]
	v_ashrrev_i32_e32 v122, 17, v122
	s_waitcnt vmcnt(7)
	v_mfma_f32_16x16x16_f16 v[60:63], v[72:73], v[68:69], v[60:63]

.Lw2b119:
	v_cmp_ne_u32_e32 vcc, v122, v115
	s_cmp_lg_u64 vcc, 0
	s_cselect_b64 s[14:15], -1, 0
	v_mfma_f32_16x16x16_f16 v[56:59], v[72:73], v[70:71], v[56:59]
	s_and_b64 s[18:19], s[14:15], vcc
	s_and_saveexec_b64 s[14:15], s[18:19]
	s_cbranch_execz .LBB2_64
	v_cmp_gt_i32_e32 vcc, 16, v115
	s_and_saveexec_b64 s[18:19], vcc
	s_cbranch_execz .LBB2_63
	s_nop 1
	v_cvt_pk_f16_f32 v59, v58, v59
	v_cvt_pk_f16_f32 v58, v56, v57

.LBB2_63:
	s_or_b64 exec, exec, s[18:19]
	s_nop 0
	v_mov_b32_e32 v56, 0
	v_mov_b32_e32 v115, v122
	v_mov_b32_e32 v57, v56
	v_mov_b32_e32 v58, v56

.Lw2b121:
	v_mov_b32_e32 v59, v56
	v_mov_b32_e32 v60, v56
	v_mov_b32_e32 v61, v56
	v_mov_b32_e32 v62, v56
	v_mov_b32_e32 v63, v56
.LBB2_64:
	s_or_b64 exec, exec, s[14:15]
	v_ashrrev_i32_e32 v68, 17, v121
	s_waitcnt vmcnt(6)
	v_mfma_f32_16x16x16_f16 v[60:63], v[72:73], v[64:65], v[60:63]
	v_cmp_ne_u32_e32 vcc, v68, v115
	s_cmp_lg_u64 vcc, 0
	s_cselect_b64 s[14:15], -1, 0
	v_mfma_f32_16x16x16_f16 v[56:59], v[72:73], v[66:67], v[56:59]

.Lw2b124:
	s_or_b64 exec, exec, s[14:15]
	v_ashrrev_i32_e32 v64, 17, v120
	s_waitcnt vmcnt(5)
	v_mfma_f32_16x16x16_f16 v[60:63], v[72:73], v[52:53], v[60:63]
	v_cmp_ne_u32_e32 vcc, v64, v115
	s_cmp_lg_u64 vcc, 0
	s_cselect_b64 s[14:15], -1, 0
	v_mfma_f32_16x16x16_f16 v[52:55], v[72:73], v[54:55], v[56:59]
	s_and_b64 s[18:19], s[14:15], vcc
	s_and_saveexec_b64 s[14:15], s[18:19]
	s_cbranch_execz .LBB2_72
	v_cmp_gt_i32_e32 vcc, 16, v115
	s_and_saveexec_b64 s[18:19], vcc

.Lw2b126:
	s_nop 0
	v_mov_b32_e32 v52, 0
	v_mov_b32_e32 v115, v64
	v_mov_b32_e32 v53, v52
	v_mov_b32_e32 v54, v52
	v_mov_b32_e32 v55, v52
	v_mov_b32_e32 v60, v52
	v_mov_b32_e32 v61, v52
	v_mov_b32_e32 v62, v52
	v_mov_b32_e32 v63, v52
.LBB2_72:
	s_or_b64 exec, exec, s[14:15]
	v_ashrrev_i32_e32 v64, 17, v119
	s_waitcnt vmcnt(4)
	v_mfma_f32_16x16x16_f16 v[56:59], v[72:73], v[48:49], v[60:63]

.LBB2_76:
	s_or_b64 exec, exec, s[14:15]
	v_ashrrev_i32_e32 v60, 17, v118
	s_waitcnt vmcnt(3)
	v_mfma_f32_16x16x16_f16 v[52:55], v[72:73], v[44:45], v[56:59]
	v_cmp_ne_u32_e32 vcc, v60, v115
	s_cmp_lg_u64 vcc, 0
	s_cselect_b64 s[14:15], -1, 0
	v_mfma_f32_16x16x16_f16 v[44:47], v[72:73], v[46:47], v[48:51]

.Lw2b132:
	s_or_b64 exec, exec, s[14:15]
	v_ashrrev_i32_e32 v56, 17, v117
	s_waitcnt vmcnt(2)
	v_mfma_f32_16x16x16_f16 v[48:51], v[72:73], v[40:41], v[52:55]
	v_cmp_ne_u32_e32 vcc, v56, v115
	s_cmp_lg_u64 vcc, 0
	s_cselect_b64 s[14:15], -1, 0
	v_mfma_f32_16x16x16_f16 v[40:43], v[72:73], v[42:43], v[44:47]
	s_and_b64 s[18:19], s[14:15], vcc
	s_and_saveexec_b64 s[14:15], s[18:19]
	s_cbranch_execz .LBB2_84
	v_cmp_gt_i32_e32 vcc, 16, v115
	s_and_saveexec_b64 s[18:19], vcc

.LBB2_84:
	s_or_b64 exec, exec, s[14:15]
	v_ashrrev_i32_e32 v52, 17, v116
	s_waitcnt vmcnt(1)
	v_mfma_f32_16x16x16_f16 v[44:47], v[72:73], v[36:37], v[48:51]

.LBB2_89:
	v_mov_b32_e32 v113, v32
	v_mov_b32_e32 v116, v114
	s_branch .LBB2_20
.LBB2_90:
.Lw2t138:
	s_cbranch_execz .Lw2c138
.Lw2b138:
	v_cmp_gt_i32_e32 vcc, 16, v107
	s_and_saveexec_b64 s[14:15], vcc
	s_cbranch_execz .LBB2_15
	v_cvt_pk_f16_f32 v35, v111, v109
	v_cvt_pk_f16_f32 v34, v112, v110
	v_cvt_pk_f16_f32 v33, v106, v104
	v_cvt_pk_f16_f32 v32, v108, v105
	v_mad_u64_u32 v[36:37], s[16:17], v107, s20, v[76:77]
	ds_write_b128 v36, v[32:35]
